# attention pick prologue: first K/V tile DMAs (K0,V0,K1) and Q fragment loads issued right after the schedule decode, overlapping the key-bias copy round trip (same relative order, counted waits unchan
# baseline (speedup 1.0000x reference)
.LBB0_1689:
	s_lshl_b32 s9, s47, 8
	s_sub_i32 s30, s9, s95
	s_and_b32 s8, s47, 1
	s_addk_i32 s30, 0xff
	s_add_i32 s9, s9, s95
	s_cmp_eq_u32 s8, 0
	s_cselect_b32 s8, s9, s30
	s_lshl_b32 s8, s8, 2
	s_add_i32 s8, s8, 0
	s_add_i32 s8, s8, 0x1d100
	v_mov_b32_e32 v2, s8
	ds_read_b32 v2, v2
	s_waitcnt lgkmcnt(0)
	v_readfirstlane_b32 s8, v2
	s_cmp_eq_u32 s8, 0
	s_cbranch_scc1 .LBB0_1688
	s_and_b32 s30, s8, 0x3ff
	s_lshl_b32 s9, s30, 2
	s_add_i32 s9, s9, 0
	s_add_i32 s9, s9, 0x1f100
	v_mov_b32_e32 v2, s9
	ds_read_b32 v2, v2
	s_and_b32 s42, s8, 31
	s_lshl_b32 s9, s42, 2
	s_or_b32 s9, s9, 1
	s_bfe_u32 s43, s8, 0x2000a
	s_waitcnt lgkmcnt(0)
	v_readfirstlane_b32 s44, v2
	s_and_b32 s34, s44, 0xff
	s_sub_i32 s9, s9, s34
	s_ashr_i32 s9, s9, 1
	s_ashr_i32 s49, s8, 12
	s_and_b32 s9, s9, -2
	s_cmp_eq_u32 s43, 2
	s_cselect_b32 s41, s9, 0
	s_lshl_b32 s40, s49, 6
	s_add_i32 s41, s41, s34
	v_readfirstlane_b32 s52, v0
	s_lshr_b32 s34, s30, 9
	s_lshr_b32 s48, s52, 6
	s_lshr_b32 s35, s30, 5
	s_lshl_b32 s35, s35, 7
	s_and_b32 s35, s35, 0x780
	s_mul_i32 s36, s34, 0x2040
	s_lshl_b32 s38, s41, 6
	s_ashr_i32 s39, s38, 31
	s_add_u32 s36, s36, s38
	s_addc_u32 s37, 0, s39
	s_lshl_b64 s[36:37], s[36:37], 11
	s_add_u32 s38, s26, s36
	s_addc_u32 s39, s27, s37
	s_add_u32 s38, s38, s35
	s_addc_u32 s39, s39, 0
	s_add_u32 s36, s58, s36
	s_addc_u32 s37, s59, s37
	s_add_u32 s36, s36, s35
	s_addc_u32 s37, s37, 0
	v_lshl_add_u64 v[244:245], s[38:39], 0, v[208:209]
	s_lshl_b32 s38, s48, 4
	s_mov_b32 s39, 0
	v_lshl_add_u64 v[244:245], v[244:245], 0, s[38:39]
	s_lshr_b32 s45, s52, 2
	v_and_or_b32 v248, s45, 48, v228
	v_lshlrev_b32_e32 v248, 11, v248
	v_mov_b32_e32 v249, 0
	v_lshl_add_u64 v[248:249], s[36:37], 0, v[248:249]
	s_and_b32 s38, s45, 0x3fffffc0
	v_lshl_add_u64 v[248:249], v[248:249], 0, s[38:39]
	v_mov_b32_e32 v242, v212
	v_mov_b32_e32 v243, 0
	v_lshl_add_u64 v[248:249], v[248:249], 0, v[242:243]
	s_lshl_b32 s50, s48, 10
	s_mov_b32 s51, m0
	s_mov_b32 m0, s50
	s_nop 0
	global_load_lds_dwordx4 v[244:245], off
	s_add_i32 s45, s50, 0x6000
	s_mov_b32 m0, s45
	s_nop 0
	global_load_lds_dwordx4 v[248:249], off
	v_lshl_add_u64 v[244:245], v[244:245], 0, s[12:13]
	s_add_i32 s45, s50, 0x2000
	s_mov_b32 m0, s45
	s_nop 0
	global_load_lds_dwordx4 v[244:245], off
	s_mov_b32 m0, s51
	s_lshl_b32 s36, s34, 13
	s_lshl_b32 s37, s42, 8
	s_or_b32 s36, s36, s37
	s_lshl_b32 s37, s48, 5
	s_add_i32 s36, s36, s37
	s_mov_b32 s37, 0
	s_lshl_b64 s[36:37], s[36:37], 11
	s_add_u32 s36, s28, s36
	s_addc_u32 s37, s29, s37
	s_add_u32 s36, s36, s35
	s_addc_u32 s37, s37, 0
	global_load_dwordx4 v[114:117], v238, s[36:37]
	global_load_dwordx4 v[118:121], v238, s[36:37] offset:32
	global_load_dwordx4 v[122:125], v238, s[36:37] offset:64
	global_load_dwordx4 v[126:129], v238, s[36:37] offset:96
	v_mov_b32_e32 v246, s30
	v_lshrrev_b32_e32 v246, 5, v246
	v_mul_u32_u24_e32 v246, 0x8100, v246
	v_lshl_add_u32 v246, s42, 10, v246
	v_lshl_add_u32 v246, v0, 2, v246
	global_load_dword v247, v246, s[54:55] offset:256
	v_cmp_gt_i32_e32 vcc, s40, v252
	s_barrier
	s_and_saveexec_b64 s[34:35], vcc
	s_cbranch_execz .LBB0_1693
	s_lshl_b32 s38, s41, 6
	s_ashr_i32 s39, s38, 31
	s_cmp_lg_u32 s43, 1
	s_cselect_b64 s[36:37], -1, 0
	s_bfe_u32 s8, s8, 0x50005
	s_lshl_b32 s45, s9, 6
	s_mul_i32 s48, s8, 0x8100
	s_lshl_b64 s[8:9], s[38:39], 2
	s_add_u32 s8, s48, s8
	s_addc_u32 s9, 0, s9
	v_lshl_add_u64 v[2:3], v[210:211], 0, s[8:9]
	s_mov_b64 s[38:39], 0
	v_mov_b32_e32 v4, v236
	v_mov_b32_e32 v5, v252

.LBB0_1698:
	s_lshr_b32 s30, s30, 9
	s_cmp_lg_u32 s43, 1
	s_cselect_b64 s[38:39], -1, 0
	s_cmp_eq_u32 s43, 1
	v_readfirstlane_b32 s50, v0
	s_cselect_b64 s[8:9], -1, 0
	s_lshr_b32 s48, s50, 6
	s_lshl_b32 s35, s30, 13
	s_mul_i32 s44, s30, 0x2040
	s_lshl_b32 s30, s42, 8
	s_or_b32 s30, s35, s30
	s_lshl_b32 s52, s48, 5
	s_add_i32 s30, s30, s52
	s_lshl_b64 s[42:43], s[30:31], 11
	s_add_u32 s30, s28, s42
	s_addc_u32 s35, s29, s43
	s_lshl_b32 s34, s34, 7
	s_and_b32 s51, s34, 0x780
	s_add_u32 s34, s30, s51
	s_addc_u32 s35, s35, 0
	s_lshl_b32 s30, s41, 6
	s_ashr_i32 s41, s30, 31
	s_add_u32 s42, s44, s30
	s_addc_u32 s43, 0, s41
	s_lshl_b64 s[42:43], s[42:43], 11
	s_add_u32 s30, s26, s42
	s_addc_u32 s41, s27, s43
	s_add_u32 s44, s30, s51
	s_addc_u32 s45, s41, 0
	s_add_u32 s30, s58, s42
	s_addc_u32 s41, s59, s43
	s_add_u32 s42, s30, s51
	s_addc_u32 s43, s41, 0
	v_lshl_add_u64 v[2:3], s[44:45], 0, v[208:209]
	s_lshl_b32 s30, s48, 4
	v_lshl_add_u64 v[214:215], v[2:3], 0, s[30:31]
	s_lshr_b32 s30, s50, 2
	v_and_or_b32 v2, s30, 48, v228
	v_lshlrev_b32_e32 v196, 11, v2
	v_lshl_add_u64 v[2:3], s[42:43], 0, v[196:197]
	s_and_b32 s30, s30, 0x3fffffc0
	v_lshl_add_u64 v[2:3], v[2:3], 0, s[30:31]
	s_lshl_b32 s30, s48, 10
	s_cmp_lg_u32 0, -1
	s_cselect_b32 s41, 0, 0
	v_mov_b32_e32 v213, v197
	s_add_i32 s50, s30, s41
	v_lshl_add_u64 v[34:35], v[2:3], 0, v[212:213]
	s_add_i32 s51, s50, 0x6000
	v_lshl_add_u64 v[2:3], v[214:215], 0, s[12:13]
	s_add_i32 s41, s50, 0x2000
	v_or_b32_e32 v196, s52, v205
	v_lshl_add_u32 v2, v196, 2, 0
	v_add_u32_e32 v4, 0x20100, v2
	v_lshl_add_u64 v[2:3], v[214:215], 0, s[14:15]
	s_add_i32 s41, s50, 0x4000
	ds_read_b32 v213, v4
	s_mov_b32 s42, m0
	s_mov_b32 m0, s41
	s_nop 0
	global_load_lds_dwordx4 v[2:3], off
	s_mov_b32 m0, s42
	s_waitcnt vmcnt(3) lgkmcnt(0)
	s_barrier
	ds_read_b128 v[2:5], v233
	ds_read_b128 v[6:9], v233 offset:32
	ds_read_b128 v[36:39], v233 offset:128
	ds_read_b128 v[40:43], v233 offset:160
	ds_read_b128 v[10:13], v233 offset:64
	ds_read_b128 v[14:17], v233 offset:96
	ds_read_b128 v[44:47], v233 offset:192
	ds_read_b128 v[48:51], v233 offset:224
	ds_read_b128 v[52:55], v232 offset:512
	ds_read_b128 v[56:59], v232
	s_cmp_gt_i32 s49, 4
	s_waitcnt lgkmcnt(4)
	v_sub_f32_e32 v33, v213, v17
	v_sub_f32_e32 v32, v213, v16
	v_sub_f32_e32 v31, v213, v15
	v_sub_f32_e32 v30, v213, v14
	v_sub_f32_e32 v29, v213, v13
	v_sub_f32_e32 v28, v213, v12
	v_sub_f32_e32 v27, v213, v11
	v_sub_f32_e32 v26, v213, v10
	v_sub_f32_e32 v25, v213, v9
	v_sub_f32_e32 v24, v213, v8
	v_sub_f32_e32 v23, v213, v7
	v_sub_f32_e32 v22, v213, v6
	v_sub_f32_e32 v21, v213, v5
	v_sub_f32_e32 v20, v213, v4
	v_sub_f32_e32 v19, v213, v3
	v_sub_f32_e32 v18, v213, v2
	v_sub_f32_e32 v5, v213, v39
	v_sub_f32_e32 v4, v213, v38
	v_sub_f32_e32 v3, v213, v37
	v_sub_f32_e32 v2, v213, v36
	ds_read_b128 v[36:39], v232 offset:2048
	s_waitcnt lgkmcnt(3)
	v_sub_f32_e32 v17, v213, v51
	v_sub_f32_e32 v16, v213, v50
	v_sub_f32_e32 v15, v213, v49
	v_sub_f32_e32 v14, v213, v48
	v_sub_f32_e32 v13, v213, v47
	v_sub_f32_e32 v12, v213, v46
	v_sub_f32_e32 v11, v213, v45
	v_sub_f32_e32 v10, v213, v44
	v_sub_f32_e32 v9, v213, v43
	v_sub_f32_e32 v8, v213, v42
	v_sub_f32_e32 v7, v213, v41
	v_sub_f32_e32 v6, v213, v40
	s_cselect_b64 s[42:43], -1, 0
	s_or_b64 s[8:9], s[42:43], s[8:9]
	s_and_b64 vcc, exec, s[8:9]
	s_waitcnt vmcnt(3) lgkmcnt(1)
	v_mfma_f32_32x32x16_bf16 v[18:33], v[56:59], v[114:117], v[18:33]
	s_waitcnt vmcnt(2) lgkmcnt(0)
	v_mfma_f32_32x32x16_bf16 v[18:33], v[36:39], v[118:121], v[18:33]
	ds_read_b128 v[36:39], v232 offset:2560
	v_mfma_f32_32x32x16_bf16 v[2:17], v[52:55], v[114:117], v[2:17]
	s_waitcnt lgkmcnt(0)
	v_mfma_f32_32x32x16_bf16 v[2:17], v[36:39], v[118:121], v[2:17]
	ds_read_b128 v[36:39], v232 offset:4096
	s_waitcnt vmcnt(1) lgkmcnt(0)
	v_mfma_f32_32x32x16_bf16 v[18:33], v[36:39], v[122:125], v[18:33]
	ds_read_b128 v[36:39], v232 offset:4608
	s_waitcnt lgkmcnt(0)
	v_mfma_f32_32x32x16_bf16 v[2:17], v[36:39], v[122:125], v[2:17]
	ds_read_b128 v[36:39], v232 offset:6144
	s_waitcnt vmcnt(0) lgkmcnt(0)
	v_mfma_f32_32x32x16_bf16 v[18:33], v[36:39], v[126:129], v[18:33]
	ds_read_b128 v[36:39], v232 offset:6656
	s_waitcnt lgkmcnt(0)
	v_mfma_f32_32x32x16_bf16 v[2:17], v[36:39], v[126:129], v[2:17]
	s_nop 15
	s_nop 7
	s_cbranch_vccnz .LBB0_1700
	v_subrev_u32_e32 v36, s40, v231
	v_add_u32_e32 v38, 0x120, v36
	v_add_u32_e32 v37, 0x100, v36
	v_cmp_le_u32_e32 vcc, v38, v196
	s_nop 6
	v_cndmask_b32_e32 v2, v240, v2, vcc
	v_cmp_lt_u32_e32 vcc, v37, v196
	s_nop 1
	v_cndmask_b32_e32 v19, v240, v19, vcc
	v_cmp_le_u32_e32 vcc, v37, v196
	v_add_u32_e32 v37, 0x121, v36
	s_nop 0
	v_cndmask_b32_e32 v18, v240, v18, vcc
	v_cmp_le_u32_e32 vcc, v37, v196
	v_add_u32_e32 v37, 0x102, v36
	s_nop 0
	v_cndmask_b32_e32 v3, v240, v3, vcc
	v_cmp_le_u32_e32 vcc, v37, v196
	v_add_u32_e32 v37, 0x122, v36
	s_nop 0
	v_cndmask_b32_e32 v20, v240, v20, vcc
	v_cmp_le_u32_e32 vcc, v37, v196
	v_add_u32_e32 v37, 0x103, v36
	s_nop 0
	v_cndmask_b32_e32 v4, v240, v4, vcc
	v_cmp_le_u32_e32 vcc, v37, v196
	v_add_u32_e32 v37, 0x123, v36
	s_nop 0
	v_cndmask_b32_e32 v21, v240, v21, vcc
	v_cmp_le_u32_e32 vcc, v37, v196
	v_add_u32_e32 v37, 0x108, v36
	s_nop 0
	v_cndmask_b32_e32 v5, v240, v5, vcc
	v_cmp_le_u32_e32 vcc, v37, v196
	v_add_u32_e32 v37, 0x128, v36
	s_nop 0
	v_cndmask_b32_e32 v22, v240, v22, vcc
	v_cmp_le_u32_e32 vcc, v37, v196
	v_add_u32_e32 v37, 0x109, v36
	s_nop 0
	v_cndmask_b32_e32 v6, v240, v6, vcc
	v_cmp_le_u32_e32 vcc, v37, v196
	v_add_u32_e32 v37, 0x129, v36
	s_nop 0
	v_cndmask_b32_e32 v23, v240, v23, vcc
	v_cmp_le_u32_e32 vcc, v37, v196
	v_add_u32_e32 v37, 0x10a, v36
	s_nop 0
	v_cndmask_b32_e32 v7, v240, v7, vcc
	v_cmp_le_u32_e32 vcc, v37, v196
	v_add_u32_e32 v37, 0x12a, v36
	s_nop 0
	v_cndmask_b32_e32 v24, v240, v24, vcc
	v_cmp_le_u32_e32 vcc, v37, v196
	v_add_u32_e32 v37, 0x10b, v36
	s_nop 0
	v_cndmask_b32_e32 v8, v240, v8, vcc
	v_cmp_le_u32_e32 vcc, v37, v196
	v_add_u32_e32 v37, 0x12b, v36
	s_nop 0
	v_cndmask_b32_e32 v25, v240, v25, vcc
	v_cmp_le_u32_e32 vcc, v37, v196
	v_add_u32_e32 v37, 0x110, v36
	s_nop 0
	v_cndmask_b32_e32 v9, v240, v9, vcc
	v_cmp_le_u32_e32 vcc, v37, v196
	v_add_u32_e32 v37, 0x130, v36
	s_nop 0
	v_cndmask_b32_e32 v26, v240, v26, vcc
	v_cmp_le_u32_e32 vcc, v37, v196
	v_add_u32_e32 v37, 0x111, v36
	s_nop 0
	v_cndmask_b32_e32 v10, v240, v10, vcc
	v_cmp_le_u32_e32 vcc, v37, v196
	v_add_u32_e32 v37, 0x131, v36
	s_nop 0
	v_cndmask_b32_e32 v27, v240, v27, vcc
	v_cmp_le_u32_e32 vcc, v37, v196
	v_add_u32_e32 v37, 0x112, v36
	s_nop 0
	v_cndmask_b32_e32 v11, v240, v11, vcc
	v_cmp_le_u32_e32 vcc, v37, v196
	v_add_u32_e32 v37, 0x132, v36
	s_nop 0
	v_cndmask_b32_e32 v28, v240, v28, vcc
	v_cmp_le_u32_e32 vcc, v37, v196
	v_add_u32_e32 v37, 0x113, v36
	s_nop 0
	v_cndmask_b32_e32 v12, v240, v12, vcc
	v_cmp_le_u32_e32 vcc, v37, v196
	v_add_u32_e32 v37, 0x133, v36
	s_nop 0
	v_cndmask_b32_e32 v29, v240, v29, vcc
	v_cmp_le_u32_e32 vcc, v37, v196
	v_add_u32_e32 v37, 0x118, v36
	s_nop 0
	v_cndmask_b32_e32 v13, v240, v13, vcc
	v_cmp_le_u32_e32 vcc, v37, v196
	v_add_u32_e32 v37, 0x138, v36
	s_nop 0
	v_cndmask_b32_e32 v30, v240, v30, vcc
	v_cmp_le_u32_e32 vcc, v37, v196
	v_add_u32_e32 v37, 0x119, v36
	s_nop 0
	v_cndmask_b32_e32 v14, v240, v14, vcc
	v_cmp_le_u32_e32 vcc, v37, v196
	v_add_u32_e32 v37, 0x139, v36
	s_nop 0
	v_cndmask_b32_e32 v31, v240, v31, vcc
	v_cmp_le_u32_e32 vcc, v37, v196
	v_add_u32_e32 v37, 0x11a, v36
	s_nop 0
	v_cndmask_b32_e32 v15, v240, v15, vcc
	v_cmp_le_u32_e32 vcc, v37, v196
	v_add_u32_e32 v37, 0x13a, v36
	s_nop 0
	v_cndmask_b32_e32 v32, v240, v32, vcc
	v_cmp_le_u32_e32 vcc, v37, v196
	v_add_u32_e32 v37, 0x11b, v36
	v_add_u32_e32 v36, 0x13b, v36
	v_cndmask_b32_e32 v16, v240, v16, vcc
	v_cmp_le_u32_e32 vcc, v37, v196
	s_nop 1
	v_cndmask_b32_e32 v33, v240, v33, vcc
	v_cmp_le_u32_e32 vcc, v36, v196
	s_nop 1
	v_cndmask_b32_e32 v17, v240, v17, vcc
